# plus nt on P3 M1 inputs (V DMA, conv'd k) and P4 old-version OST/ML state loads
# baseline (speedup 1.0000x reference)
; #define LAS __attribute__((address_space(3)))
; DI float log_sigmoid(float x) { return fminf(x, 0.f) - log1pf(__expf(-fabsf(x))); }
; DI void mlstm_m1_unit(Frame& F, int u) {
;     const int bh = u >> 7, c = u & 127, b = bh >> 2, hd = bh & 3;
;     const int tok0 = b * SEQ + c * 128;
;     const float* GATES = (const float*)(F.ws + WS_GATES);
;     LAS float* mf = (LAS float*)(F.lds + MISC_OFF);
;     LAS unsigned char* imgK = F.lds, *imgV0 = F.lds + 32768, *imgV1 = F.lds + 65536;
;     const int lane = F.lane;
;     const bf16* KC = (const bf16*)(F.ws + WS_KC); const bf16* PROJ = (const bf16*)(F.ws + WS_PROJ);
;     dma_img128(imgV0, PROJ + (size_t)tok0 * NPROJ + COL_MV + hd * 256, NPROJ, F.wave, lane);
;     dma_img128(imgV1, PROJ + (size_t)tok0 * NPROJ + COL_MV + hd * 256 + 128, NPROJ, F.wave, lane);
;     asm volatile("" ::: "memory");
;     u32x4 kreg[4];
; #pragma unroll
;     for (int it = 0; it < 4; ++it) { const int idx = F.tid + NTHR * it, row = idx >> 4, ch = idx & 15; kreg[it] = *(const u32x4*)(KC + (size_t)(tok0 + row) * 512 + hd * 128 + 8 * ch); }
;     if (F.wave == 0) {
;         const int s0 = 2 * lane;
;         const float ig0 = GATES[(size_t)(tok0 + s0) * 8 + hd], fg0 = GATES[(size_t)(tok0 + s0) * 8 + 4 + hd];
;         const float ig1 = GATES[(size_t)(tok0 + s0 + 1) * 8 + hd], fg1 = GATES[(size_t)(tok0 + s0 + 1) * 8 + 4 + hd];
;         const float lf0 = log_sigmoid(fg0), lf1 = log_sigmoid(fg1);
.LBB0_352:
	s_lshl_b32 s1, s24, 5
	s_lshl_b32 s20, s24, 7
	s_and_b32 s1, s1, 0xffffc000
	s_and_b32 s20, s20, 0x3f80
	s_or_b32 s1, s1, s20
	s_bfe_u32 s0, s24, 0x20007
	s_mul_i32 s25, s1, 0x3000
	s_mul_hi_i32 s20, s1, 0x3000
	s_add_u32 s25, s94, s25
	s_addc_u32 s55, s95, s20
	s_lshl_b32 s20, s0, 8
	s_lshl_b32 s56, s0, 9
	s_add_u32 s25, s25, s56
	s_addc_u32 s55, s55, 0
	s_add_u32 s56, s25, 0x3c002000
	s_addc_u32 s57, s55, 0
	v_lshl_add_u64 v[2:3], s[56:57], 0, v[66:67]
	s_mov_b32 m0, s47
	v_lshl_add_u64 v[2:3], v[2:3], 0, v[68:69]
	v_lshl_add_u64 v[4:5], s[56:57], 0, v[70:71]
	v_mov_b32_e32 v97, v69
	global_load_lds_dwordx4 v[2:3], off nt
	v_lshl_add_u64 v[4:5], v[4:5], 0, v[96:97]
	s_mov_b32 m0, s48
	v_lshl_add_u64 v[6:7], s[56:57], 0, v[72:73]
	v_mov_b32_e32 v99, v69
	global_load_lds_dwordx4 v[4:5], off nt
	v_lshl_add_u64 v[6:7], v[6:7], 0, v[98:99]
	s_mov_b32 m0, s49
	v_lshl_add_u64 v[8:9], s[56:57], 0, v[74:75]
	v_mov_b32_e32 v101, v69
	global_load_lds_dwordx4 v[6:7], off nt
	v_lshl_add_u64 v[8:9], v[8:9], 0, v[100:101]
	s_mov_b32 m0, s50
	v_lshl_add_u64 v[2:3], v[2:3], 0, s[22:23]
	global_load_lds_dwordx4 v[8:9], off nt
	s_mov_b32 m0, s51
	s_andn2_b64 vcc, exec, s[16:17]
	global_load_lds_dwordx4 v[2:3], off nt
	v_lshl_add_u64 v[2:3], v[4:5], 0, s[22:23]
	s_mov_b32 m0, s52
	v_or_b32_e32 v4, s1, v110
	global_load_lds_dwordx4 v[2:3], off nt
	v_lshl_add_u64 v[2:3], v[6:7], 0, s[22:23]
	s_mov_b32 m0, s53
	v_or_b32_e32 v6, s1, v111
	global_load_lds_dwordx4 v[2:3], off nt
	v_lshl_add_u64 v[2:3], v[8:9], 0, s[22:23]
	s_mov_b32 m0, s54
	v_ashrrev_i32_e32 v5, 31, v4
	v_ashrrev_i32_e32 v7, 31, v6
	global_load_lds_dwordx4 v[2:3], off nt
	v_lshl_add_u64 v[2:3], v[76:77], 0, s[20:21]
	v_lshlrev_b64 v[4:5], 10, v[4:5]
	v_lshlrev_b64 v[6:7], 10, v[6:7]
	v_lshl_add_u64 v[4:5], v[2:3], 0, v[4:5]
	v_lshl_add_u64 v[6:7], v[2:3], 0, v[6:7]
	global_load_dwordx4 v[14:17], v[4:5], off nt
	global_load_dwordx4 v[10:13], v[6:7], off nt
	v_or_b32_e32 v4, s1, v112
	v_or_b32_e32 v6, s1, v113
	v_ashrrev_i32_e32 v5, 31, v4
	v_ashrrev_i32_e32 v7, 31, v6
	v_lshlrev_b64 v[4:5], 10, v[4:5]
	v_lshlrev_b64 v[6:7], 10, v[6:7]
	v_lshl_add_u64 v[4:5], v[2:3], 0, v[4:5]
	v_lshl_add_u64 v[2:3], v[2:3], 0, v[6:7]
	global_load_dwordx4 v[6:9], v[4:5], off nt
	s_nop 0
	global_load_dwordx4 v[2:5], v[2:3], off nt
	s_cbranch_vccnz .LBB0_356
	v_or_b32_e32 v18, s1, v114
	v_ashrrev_i32_e32 v19, 31, v18
	v_lshlrev_b64 v[20:21], 5, v[18:19]
	v_lshl_add_u64 v[20:21], s[18:19], 0, v[20:21]
	s_lshl_b32 s20, s0, 2
	v_lshl_add_u64 v[20:21], v[20:21], 0, s[20:21]
	v_or_b32_e32 v18, 1, v18
	global_load_dword v22, v[20:21], off offset:16
	v_ashrrev_i32_e32 v19, 31, v18
	v_lshlrev_b64 v[18:19], 5, v[18:19]
	v_lshl_add_u64 v[18:19], s[18:19], 0, v[18:19]
	v_lshl_add_u64 v[18:19], v[18:19], 0, s[20:21]
	global_load_dword v23, v[18:19], off offset:16
	s_nop 0
	global_load_dword v20, v[20:21], off
	s_nop 0
	global_load_dword v21, v[18:19], off
	s_waitcnt vmcnt(0)
	v_mul_f32_e64 v19, |v22|, s42
	v_exp_f32_e32 v24, v19
	v_max_f32_e32 v18, v22, v22
	v_mul_f32_e64 v19, |v23|, s42
	v_exp_f32_e32 v25, v19
	v_min_f32_e32 v22, 0, v18
	v_max_f32_e32 v18, v23, v23
	v_add_f32_e32 v26, 1.0, v24
	v_min_f32_e32 v23, 0, v18
	v_add_f32_e32 v27, -1.0, v26
	v_frexp_mant_f32_e32 v28, v26
	v_cvt_f64_f32_e32 v[18:19], v26
	v_add_f32_e32 v29, 1.0, v25
	v_sub_f32_e32 v30, v27, v26
	v_frexp_exp_i32_f64_e32 v31, v[18:19]
	v_cmp_gt_f32_e32 vcc, s43, v28
	v_sub_f32_e32 v27, v24, v27
	v_add_f32_e32 v32, -1.0, v29
	v_frexp_mant_f32_e32 v33, v29
	v_cvt_f64_f32_e32 v[18:19], v29
	v_add_f32_e32 v30, 1.0, v30
	v_subbrev_co_u32_e32 v28, vcc, 0, v31, vcc
	v_sub_f32_e32 v31, v32, v29
	v_frexp_exp_i32_f64_e32 v18, v[18:19]
	v_add_f32_e32 v19, v27, v30
	v_sub_u32_e32 v27, 0, v28
	v_cmp_gt_f32_e32 vcc, s43, v33
	v_sub_f32_e32 v32, v25, v32
	v_cvt_f32_i32_e32 v28, v28
	v_add_f32_e32 v30, 1.0, v31
	v_subbrev_co_u32_e32 v18, vcc, 0, v18, vcc
	v_ldexp_f32 v26, v26, v27
	v_ldexp_f32 v19, v19, v27
	v_add_f32_e32 v27, v32, v30
	v_sub_u32_e32 v30, 0, v18
	v_add_f32_e32 v31, -1.0, v26
	v_add_f32_e32 v32, 1.0, v26
	v_ldexp_f32 v29, v29, v30
	v_ldexp_f32 v27, v27, v30
	v_add_f32_e32 v30, 1.0, v31
	v_add_f32_e32 v33, -1.0, v32
	v_sub_f32_e32 v30, v26, v30
	v_sub_f32_e32 v26, v26, v33
	v_mul_f32_e32 v33, 0x3f317218, v28
	v_add_f32_e32 v30, v19, v30
	v_add_f32_e32 v19, v19, v26
	v_fma_f32 v26, v28, s44, -v33
	v_add_f32_e32 v36, v31, v30
	v_add_f32_e32 v37, v32, v19
	v_fmac_f32_e32 v26, 0xb102e308, v28
	v_sub_f32_e32 v28, v36, v31
	v_sub_f32_e32 v31, v37, v32
	v_rcp_f32_e32 v32, v37
	v_add_f32_e32 v38, v33, v26
	v_sub_f32_e32 v28, v30, v28
	v_sub_f32_e32 v30, v38, v33
	v_sub_f32_e32 v26, v26, v30
	v_mul_f32_e32 v30, v36, v32
	v_sub_f32_e32 v19, v19, v31
	v_mul_f32_e32 v31, v37, v30
	v_fma_f32 v33, v30, v37, -v31
	v_fmac_f32_e32 v33, v30, v19
	v_add_f32_e32 v39, v31, v33
	v_sub_f32_e32 v40, v36, v39
	v_sub_f32_e32 v31, v39, v31
	v_sub_f32_e32 v36, v36, v40
	v_sub_f32_e32 v31, v31, v33
	v_sub_f32_e32 v33, v36, v39
	v_add_f32_e32 v28, v28, v33
	v_add_f32_e32 v28, v31, v28
	v_add_f32_e32 v31, v40, v28
	v_mul_f32_e32 v33, v32, v31
	v_sub_f32_e32 v36, v40, v31
	v_mul_f32_e32 v39, v37, v33
	v_add_f32_e32 v28, v28, v36
	v_add_f32_e32 v36, v30, v33
	v_fma_f32 v37, v33, v37, -v39
	v_sub_f32_e32 v30, v36, v30
	v_fmac_f32_e32 v37, v33, v19
	v_sub_f32_e32 v19, v33, v30
	v_add_f32_e32 v30, v39, v37
	v_sub_f32_e32 v33, v30, v39
	v_sub_f32_e32 v39, v31, v30
	v_sub_f32_e32 v31, v31, v39
	v_sub_f32_e32 v30, v31, v30
	v_sub_f32_e32 v33, v33, v37
	v_add_f32_e32 v28, v28, v30
	v_add_f32_e32 v28, v33, v28
	v_add_f32_e32 v28, v39, v28
	v_mul_f32_e32 v28, v32, v28
; DI float log_sigmoid(float x) { return fminf(x, 0.f) - log1pf(__expf(-fabsf(x))); }
; DI void mlstm_m1_unit(Frame& F, int u) {
;     ...
;         const float lf0 = log_sigmoid(fg0), lf1 = log_sigmoid(fg1);
;         const float b1 = scan_incl_sum(lf0 + lf1, lane), b0 = b1 - lf1;
	v_add_f32_e32 v19, v19, v28
	v_add_f32_e32 v28, v36, v19
	v_mul_f32_e32 v30, v28, v28
	v_fmamk_f32 v33, v30, 0x3e9b6dac, v138
	v_sub_f32_e32 v31, v28, v36
	v_ldexp_f32 v32, v28, 1
	v_mul_f32_e32 v28, v28, v30
	v_fmaak_f32 v30, v30, v33, 0x3f2aaada
	v_mul_f32_e32 v28, v28, v30
	v_add_f32_e32 v30, v32, v28
	v_sub_f32_e32 v19, v19, v31
	v_sub_f32_e32 v31, v30, v32
	v_ldexp_f32 v19, v19, 1
	v_sub_f32_e32 v28, v28, v31
	v_add_f32_e32 v19, v19, v28
	v_add_f32_e32 v28, v30, v19
	v_sub_f32_e32 v30, v28, v30
	v_add_f32_e32 v31, v38, v28
	v_sub_f32_e32 v19, v19, v30
	v_sub_f32_e32 v30, v31, v38
	v_sub_f32_e32 v32, v31, v30
	v_sub_f32_e32 v28, v28, v30
	v_add_f32_e32 v30, v26, v19
	v_sub_f32_e32 v32, v38, v32
	v_sub_f32_e32 v33, v30, v26
	v_add_f32_e32 v28, v28, v32
	v_sub_f32_e32 v32, v30, v33
	v_sub_f32_e32 v19, v19, v33
	v_sub_f32_e32 v26, v26, v32
	v_add_f32_e32 v28, v30, v28
	v_add_f32_e32 v19, v19, v26
	v_add_f32_e32 v26, v31, v28
	v_sub_f32_e32 v30, v26, v31
	v_sub_f32_e32 v28, v28, v30
	v_add_f32_e32 v19, v19, v28
	v_add_f32_e32 v19, v26, v19
	v_cmp_neq_f32_e32 vcc, s45, v24
	v_add_f32_e32 v34, -1.0, v29
	v_add_f32_e32 v28, 1.0, v29
	v_cndmask_b32_e32 v19, v151, v19, vcc
	v_cmp_ngt_f32_e32 vcc, -1.0, v24
	v_add_f32_e32 v35, 1.0, v34
	v_add_f32_e32 v30, -1.0, v28
	v_cndmask_b32_e32 v19, v152, v19, vcc
	v_cmp_neq_f32_e32 vcc, -1.0, v24
	v_sub_f32_e32 v35, v29, v35
	v_sub_f32_e32 v29, v29, v30
	v_cndmask_b32_e32 v19, v153, v19, vcc
	v_cmp_lt_f32_e64 vcc, |v24|, s46
	v_cvt_f32_i32_e32 v18, v18
	s_nop 0
	v_cndmask_b32_e32 v19, v19, v24, vcc
	v_sub_f32_e32 v19, v22, v19
	v_add_f32_e32 v22, v27, v35
	v_add_f32_e32 v27, v27, v29
	v_add_f32_e32 v29, v28, v27
	v_rcp_f32_e32 v30, v29
	v_add_f32_e32 v24, v34, v22
	v_sub_f32_e32 v26, v24, v34
	v_sub_f32_e32 v22, v22, v26
	v_sub_f32_e32 v26, v29, v28
	v_sub_f32_e32 v26, v27, v26
	v_mul_f32_e32 v27, v24, v30
	v_mul_f32_e32 v28, v29, v27
	v_fma_f32 v31, v27, v29, -v28
	v_fmac_f32_e32 v31, v27, v26
	v_add_f32_e32 v32, v28, v31
	v_sub_f32_e32 v33, v24, v32
	v_sub_f32_e32 v24, v24, v33
	v_sub_f32_e32 v28, v32, v28
	v_sub_f32_e32 v24, v24, v32
	v_add_f32_e32 v22, v22, v24
	v_sub_f32_e32 v24, v28, v31
	v_add_f32_e32 v22, v24, v22
	v_add_f32_e32 v24, v33, v22
	v_mul_f32_e32 v28, v30, v24
	v_mul_f32_e32 v31, v29, v28
	v_fma_f32 v29, v28, v29, -v31
	v_fmac_f32_e32 v29, v28, v26
	v_sub_f32_e32 v26, v33, v24
	v_add_f32_e32 v22, v22, v26
	v_add_f32_e32 v26, v31, v29
	v_sub_f32_e32 v32, v24, v26
	v_sub_f32_e32 v24, v24, v32
	v_sub_f32_e32 v31, v26, v31
	v_sub_f32_e32 v24, v24, v26
	v_add_f32_e32 v22, v22, v24
	v_sub_f32_e32 v24, v31, v29
	v_add_f32_e32 v22, v24, v22
	v_add_f32_e32 v24, v27, v28
	v_add_f32_e32 v22, v32, v22
	v_sub_f32_e32 v26, v24, v27
	v_mul_f32_e32 v22, v30, v22
	v_sub_f32_e32 v26, v28, v26
	v_add_f32_e32 v22, v26, v22
	v_mul_f32_e32 v29, 0x3f317218, v18
	v_add_f32_e32 v26, v24, v22
	v_fma_f32 v30, v18, s44, -v29
	v_mul_f32_e32 v27, v26, v26
	v_fmac_f32_e32 v30, 0xb102e308, v18
	v_sub_f32_e32 v18, v26, v24
	v_fmamk_f32 v28, v27, 0x3e9b6dac, v138
	v_sub_f32_e32 v18, v22, v18
	v_add_f32_e32 v22, v29, v30
	v_fmaak_f32 v28, v27, v28, 0x3f2aaada
	v_sub_f32_e32 v24, v22, v29
	v_ldexp_f32 v29, v26, 1
	v_mul_f32_e32 v26, v26, v27
	v_mul_f32_e32 v26, v26, v28
	v_add_f32_e32 v27, v29, v26
	v_sub_f32_e32 v28, v27, v29
	v_ldexp_f32 v18, v18, 1
	v_sub_f32_e32 v26, v26, v28
	v_add_f32_e32 v18, v18, v26
	v_add_f32_e32 v26, v27, v18
	v_sub_f32_e32 v27, v26, v27
	v_sub_f32_e32 v18, v18, v27
	v_add_f32_e32 v27, v22, v26
	v_sub_f32_e32 v28, v27, v22
	v_sub_f32_e32 v29, v27, v28
	v_sub_f32_e32 v24, v30, v24
	v_sub_f32_e32 v22, v22, v29
	v_sub_f32_e32 v26, v26, v28
	v_add_f32_e32 v22, v26, v22
	v_add_f32_e32 v26, v24, v18
	v_sub_f32_e32 v28, v26, v24
	v_sub_f32_e32 v29, v26, v28
	v_sub_f32_e32 v24, v24, v29
	v_sub_f32_e32 v18, v18, v28
	v_add_f32_e32 v22, v26, v22
	v_add_f32_e32 v18, v18, v24
	v_add_f32_e32 v24, v27, v22
	v_sub_f32_e32 v26, v24, v27
	v_sub_f32_e32 v22, v22, v26
	v_add_f32_e32 v18, v18, v22
	v_add_f32_e32 v18, v24, v18
	v_cmp_neq_f32_e32 vcc, s45, v25
	s_nop 1
	v_cndmask_b32_e32 v18, v151, v18, vcc
	v_cmp_ngt_f32_e32 vcc, -1.0, v25
	s_nop 1
	v_cndmask_b32_e32 v18, v152, v18, vcc
	v_cmp_neq_f32_e32 vcc, -1.0, v25
	s_nop 1
	v_cndmask_b32_e32 v18, v153, v18, vcc
	v_cmp_lt_f32_e64 vcc, |v25|, s46
	s_nop 1
	v_cndmask_b32_e32 v18, v18, v25, vcc
	v_sub_f32_e32 v22, v23, v18
	v_add_f32_e32 v18, v19, v22
	v_and_b32_e32 v19, 64, v154
	v_add_u32_e32 v23, -1, v154
	v_cmp_lt_i32_e32 vcc, v23, v19
	s_nop 1
	v_cndmask_b32_e32 v23, v23, v154, vcc
	v_lshlrev_b32_e32 v23, 2, v23
	ds_bpermute_b32 v23, v23, v18
	s_waitcnt lgkmcnt(0)
; DI void mlstm_m1_unit(Frame& F, int u) {
;     ...
;         const float b1 = scan_incl_sum(lf0 + lf1, lane), b0 = b1 - lf1;
;         const float gt = __shfl(b1, 63);
;         const float a0 = gt - b0 + ig0, a1 = gt - b1 + ig1;
;         const float ml = wave_max(fmaxf(a0, a1));
;         mf[s0] = __expf(a0 - ml); mf[s0 + 1] = __expf(a1 - ml);
;         if (lane == 0) { ((float*)(F.ws + WS_SMALL + SM_G))[u] = gt; ((float*)(F.ws + WS_SMALL + SM_MLOC))[u] = ml; }
	v_add_f32_e32 v23, v18, v23
	v_cndmask_b32_e64 v18, v23, v18, s[2:3]
	v_add_u32_e32 v23, -2, v154
	v_cmp_lt_i32_e32 vcc, v23, v19
	s_nop 1
	v_cndmask_b32_e32 v23, v23, v154, vcc
	v_lshlrev_b32_e32 v23, 2, v23
	ds_bpermute_b32 v23, v23, v18
	s_waitcnt lgkmcnt(0)
	v_add_f32_e32 v23, v18, v23
	v_cndmask_b32_e64 v18, v23, v18, s[4:5]
	v_add_u32_e32 v23, -4, v154
	v_cmp_lt_i32_e32 vcc, v23, v19
	s_nop 1
	v_cndmask_b32_e32 v23, v23, v154, vcc
	v_lshlrev_b32_e32 v23, 2, v23
	ds_bpermute_b32 v23, v23, v18
	s_waitcnt lgkmcnt(0)
	v_add_f32_e32 v23, v18, v23
	v_cndmask_b32_e64 v18, v23, v18, s[6:7]
	v_add_u32_e32 v23, -8, v154
	v_cmp_lt_i32_e32 vcc, v23, v19
	s_nop 1
	v_cndmask_b32_e32 v23, v23, v154, vcc
	v_lshlrev_b32_e32 v23, 2, v23
	ds_bpermute_b32 v23, v23, v18
	s_waitcnt lgkmcnt(0)
	v_add_f32_e32 v23, v18, v23
	v_cndmask_b32_e64 v18, v23, v18, s[8:9]
	v_add_u32_e32 v23, -16, v154
	v_cmp_lt_i32_e32 vcc, v23, v19
	s_nop 1
	v_cndmask_b32_e32 v23, v23, v154, vcc
	v_lshlrev_b32_e32 v23, 2, v23
	ds_bpermute_b32 v23, v23, v18
	s_waitcnt lgkmcnt(0)
	v_add_f32_e32 v23, v18, v23
	v_cndmask_b32_e64 v18, v23, v18, s[10:11]
	v_subrev_u32_e32 v23, 32, v154
	v_cmp_lt_i32_e32 vcc, v23, v19
	v_add_u32_e32 v19, 64, v19
	s_nop 0
	v_cndmask_b32_e32 v23, v23, v154, vcc
	v_lshlrev_b32_e32 v23, 2, v23
	ds_bpermute_b32 v23, v23, v18
	s_waitcnt lgkmcnt(0)
	v_add_f32_e32 v23, v18, v23
	v_cndmask_b32_e64 v23, v23, v18, s[12:13]
	ds_bpermute_b32 v18, v155, v23
	v_sub_f32_e32 v22, v23, v22
	s_waitcnt lgkmcnt(0)
	v_sub_f32_e32 v22, v18, v22
	v_add_f32_e32 v20, v20, v22
	v_sub_f32_e32 v22, v18, v23
	v_xor_b32_e32 v23, 1, v154
	v_cmp_lt_i32_e32 vcc, v23, v19
	v_add_f32_e32 v21, v21, v22
	v_max_f32_e32 v22, v20, v21
	v_cndmask_b32_e32 v23, v154, v23, vcc
	v_lshlrev_b32_e32 v23, 2, v23
	ds_bpermute_b32 v23, v23, v22
	s_waitcnt lgkmcnt(0)
	v_max_f32_e32 v23, v23, v23
	v_max_f32_e32 v22, v22, v23
	v_xor_b32_e32 v23, 2, v154
	v_cmp_lt_i32_e32 vcc, v23, v19
	s_nop 1
	v_cndmask_b32_e32 v23, v154, v23, vcc
	v_lshlrev_b32_e32 v23, 2, v23
	ds_bpermute_b32 v23, v23, v22
	s_waitcnt lgkmcnt(0)
	v_max_f32_e32 v23, v23, v23
	v_max_f32_e32 v22, v22, v23
	v_xor_b32_e32 v23, 4, v154
	v_cmp_lt_i32_e32 vcc, v23, v19
	s_nop 1
	v_cndmask_b32_e32 v23, v154, v23, vcc
	v_lshlrev_b32_e32 v23, 2, v23
	ds_bpermute_b32 v23, v23, v22
	s_waitcnt lgkmcnt(0)
	v_max_f32_e32 v23, v23, v23
	v_max_f32_e32 v22, v22, v23
	v_xor_b32_e32 v23, 8, v154
	v_cmp_lt_i32_e32 vcc, v23, v19
	s_nop 1
	v_cndmask_b32_e32 v23, v154, v23, vcc
	v_lshlrev_b32_e32 v23, 2, v23
	ds_bpermute_b32 v23, v23, v22
	s_waitcnt lgkmcnt(0)
	v_max_f32_e32 v23, v23, v23
	v_max_f32_e32 v22, v22, v23
	v_xor_b32_e32 v23, 16, v154
	v_cmp_lt_i32_e32 vcc, v23, v19
	s_nop 1
	v_cndmask_b32_e32 v23, v154, v23, vcc
	v_lshlrev_b32_e32 v23, 2, v23
	ds_bpermute_b32 v23, v23, v22
	s_waitcnt lgkmcnt(0)
	v_max_f32_e32 v23, v23, v23
	v_max_f32_e32 v22, v22, v23
	v_xor_b32_e32 v23, 32, v154
	v_cmp_lt_i32_e32 vcc, v23, v19
	s_nop 1
	v_cndmask_b32_e32 v19, v154, v23, vcc
	v_lshlrev_b32_e32 v19, 2, v19
	ds_bpermute_b32 v19, v19, v22
	s_waitcnt lgkmcnt(0)
	v_max_f32_e32 v19, v19, v19
	v_max_f32_e32 v19, v22, v19
	v_sub_f32_e32 v20, v20, v19
	v_sub_f32_e32 v21, v21, v19
	v_mul_f32_e32 v20, 0x3fb8aa3b, v20
	v_mul_f32_e32 v21, 0x3fb8aa3b, v21
	v_exp_f32_e32 v20, v20
	v_exp_f32_e32 v21, v21
	ds_write_b64 v115, v[20:21]
	s_and_saveexec_b64 s[0:1], s[2:3]
	s_cbranch_execz .LBB0_355
	s_ashr_i32 s25, s24, 31
	s_lshl_b64 s[56:57], s[24:25], 2
	s_add_u32 s58, s27, s56
	s_addc_u32 s59, s28, s57
	s_add_u32 s56, s29, s56
	s_addc_u32 s57, s30, s57
	global_store_dword v69, v18, s[56:57]
	global_store_dword v69, v19, s[58:59]

; DI int tr_base(int rlane, int cch, int q, int p) { return img_off(rlane + q, cch + (p >> 1)) + 8 * (p & 1); }
; #define ATT_DECODE(k_, b_, hd_, res_, ib_) do { const int u_ = F.vcu + (k_) * F.G; const int bh_ = u_ >> 4, uu_ = u_ & 15; b_ = bh_ >> 3; hd_ = bh_ & 7; res_ = uu_ / BPR; ib_ = (uu_ % BPR) * 1024; } while (0)
; template <int DIL, bool FIRST, bool LAST>
; DI void attn_phase(Frame& F) {
;     ...
;     const int lane = F.lane, r = lane & 31, h = lane >> 5, g = lane >> 4, i16 = lane & 15, q4 = i16 >> 2, p4 = i16 & 3;
;     const int prow = 4 * F.wave + g, pch = i16 ^ ((g << 2) | (F.wave & 3));
;     const unsigned pdst = (unsigned)F.wave * 1024u;
;     int vB0[4], vB1[4];
; #pragma unroll
;     for (int db = 0; db < 4; ++db) { vB0[db] = tr_base(4 * h, 4 * db + 2 * (g & 1), q4, p4); vB1[db] = tr_base(8 + 4 * h, 4 * db + 2 * (g & 1), q4, p4); }
;     const int kmask = ((r & 3) << 2) | ((r >> 2) & 3);
;     __syncthreads();
;     const int nun = (F.vcu < 256) ? (255 - F.vcu) / F.G + 1 : 0;
;     if (nun > 0) {
;     ...
;         int iu = 0, ij = 0, is = 0, ib_i; const bf16* kv_i;
;         { int b_, hd_, res_; ATT_DECODE(0, b_, hd_, res_, ib_i); kv_i = HMq + HM_PLANE + ((size_t)(b_ * 8 + hd_) * SEQ + res_) * 128; }
;     ...
;         u32x4 qfr[8], on[8]; u32x2 mlx; mlx.x = 0u; mlx.y = 0u;
;     ...
;         ATT_PREFETCH(0, F.wave);
.LBB0_585:
	s_cmp_lt_i32 s72, 1
	s_cbranch_scc1 .LBB0_617
	v_writelane_b32 v254, s76, 58
	v_lshrrev_b32_e32 v2, 4, v224
	v_and_b32_e32 v3, 15, v0
	v_writelane_b32 v254, s77, 59
	s_add_u32 s76, s94, 0x6c000000
	s_addc_u32 s77, s95, 0
	v_lshlrev_b32_e32 v4, 2, v2
	s_bfe_u32 s0, s78, 0x20006
	v_bitop3_b32 v9, s0, v3, v4 bitop3:0x36
	s_add_u32 s0, s94, 0x64000000
	s_addc_u32 s1, s95, 0
	s_add_u32 s2, s94, 0xa7400000
	s_addc_u32 s3, s95, 0
	v_readlane_b32 s70, v254, 23
	s_lshl_b32 s5, s85, 10
	s_lshl_b32 s8, s70, 10
	s_bfe_u32 s4, s85, 0x30004
	s_and_b32 s75, s5, 0xc00
	v_bfe_u32 v8, v0, 2, 2
	v_lshlrev_b32_e32 v10, 2, v222
	v_lshrrev_b32_e32 v3, 3, v224
	v_and_b32_e32 v7, 12, v0
	v_lshlrev_b32_e32 v12, 3, v0
	s_add_u32 s9, s94, 0xab400000
	v_and_b32_e32 v3, 2, v3
	v_or_b32_e32 v4, v10, v8
	v_bfe_u32 v5, v0, 1, 1
	v_or_b32_e32 v11, v222, v7
	v_and_b32_e32 v12, 8, v12
	v_or_b32_e32 v13, 8, v10
	s_addc_u32 s10, s95, 0
	s_ashr_i32 s5, s85, 4
	v_or_b32_e32 v6, v3, v5
	v_lshl_or_b32 v4, v4, 8, v12
	v_or_b32_e32 v14, v13, v8
	v_lshrrev_b32_e32 v15, 2, v13
	v_bitop3_b32 v3, v3, v11, v5 bitop3:0x36
	s_and_b32 s5, s5, -8
	v_lshl_or_b32 v12, v14, 8, v12
	v_lshl_or_b32 v196, v3, 4, v4
	v_bitop3_b32 v3, v15, v6, v7 bitop3:0x36
	s_or_b32 s4, s5, s4
	v_or_b32_e32 v16, v15, v7
	v_lshl_add_u32 v197, v3, 4, v12
	v_bitop3_b32 v3, v6, v11, 4 bitop3:0x36
	s_ashr_i32 s5, s4, 31
	v_lshl_or_b32 v198, v3, 4, v4
	v_bitop3_b32 v3, v6, v16, 4 bitop3:0x36
	s_lshl_b64 s[6:7], s[4:5], 22
	v_lshl_add_u32 v199, v3, 4, v12
	v_bitop3_b32 v3, v6, v11, 8 bitop3:0x36
	v_writelane_b32 v254, s9, 51
	s_add_u32 s9, s9, s6
	v_lshl_or_b32 v200, v3, 4, v4
	v_bitop3_b32 v3, v6, v16, 8 bitop3:0x36
	v_writelane_b32 v254, s10, 52
	s_addc_u32 s10, s10, s7
	s_lshl_b64 s[6:7], s[4:5], 14
	s_lshl_b32 s4, s70, 5
	v_lshl_add_u32 v201, v3, 4, v12
	v_bitop3_b32 v3, v6, v11, 12 bitop3:0x36
	s_add_i32 s5, s75, s4
	v_lshl_or_b32 v202, v3, 4, v4
	v_bitop3_b32 v3, v6, v16, 12 bitop3:0x36
	v_lshl_or_b32 v11, s70, 2, v2
	v_lshlrev_b32_e32 v2, 2, v0
	v_or_b32_e32 v178, s5, v1
	v_mov_b32_e32 v179, 0
	v_lshl_add_u32 v203, v3, 4, v12
	v_and_b32_e32 v12, 12, v2
	s_lshr_b32 s11, s85, 2
	v_lshl_add_u64 v[2:3], v[178:179], 2, s[6:7]
	v_and_or_b32 v2, s11, 3, v2
	v_lshlrev_b64 v[4:5], 8, v[2:3]
	v_lshl_add_u64 v[6:7], s[2:3], 0, v[4:5]
	v_lshlrev_b32_e32 v178, 4, v222
	v_lshl_add_u64 v[6:7], v[6:7], 0, v[178:179]
	s_waitcnt vmcnt(8)
	global_load_dwordx4 v[82:85], v[6:7], off offset:0
	s_waitcnt vmcnt(7)
; #define ATT_DECODE(k_, b_, hd_, res_, ib_) do { const int u_ = F.vcu + (k_) * F.G; const int bh_ = u_ >> 4, uu_ = u_ & 15; b_ = bh_ >> 3; hd_ = bh_ & 7; res_ = uu_ / BPR; ib_ = (uu_ % BPR) * 1024; } while (0)
; template <int DIL, bool FIRST, bool LAST>
; DI void attn_phase(Frame& F) {
;     ...
;     const int kmask = ((r & 3) << 2) | ((r >> 2) & 3);
;     __syncthreads();
;     const int nun = (F.vcu < 256) ? (255 - F.vcu) / F.G + 1 : 0;
;     if (nun > 0) {
;     ...
;         int iu = 0, ij = 0, is = 0, ib_i; const bf16* kv_i;
;         { int b_, hd_, res_; ATT_DECODE(0, b_, hd_, res_, ib_i); kv_i = HMq + HM_PLANE + ((size_t)(b_ * 8 + hd_) * SEQ + res_) * 128; }
;     ...
;         u32x4 qfr[8], on[8]; u32x2 mlx; mlx.x = 0u; mlx.y = 0u;
;     ...
;         ATT_PREFETCH(0, F.wave);
; #pragma unroll
;         for (int jt = 0; jt < PRE; ++jt) ATT_ISSUE1();
;         int cs = 0;
;         f32x16 o[4]; float m = -1e30f, l = 0.f;
	global_load_dwordx4 v[86:89], v[6:7], off offset:32
	global_load_dwordx4 v[90:93], v[6:7], off offset:64
	global_load_dwordx4 v[94:97], v[6:7], off offset:0x60
	global_load_dwordx4 v[98:101], v[6:7], off offset:0x80
	global_load_dwordx4 v[102:105], v[6:7], off offset:0xa0
	global_load_dwordx4 v[106:109], v[6:7], off offset:0xc0
	global_load_dwordx4 v[110:113], v[6:7], off offset:0xe0
	v_lshl_add_u64 v[4:5], s[0:1], 0, v[4:5]
	v_lshl_add_u64 v[4:5], v[4:5], 0, v[178:179]
	global_load_dwordx4 v[114:117], v[4:5], off offset:0 nt
	global_load_dwordx4 v[118:121], v[4:5], off offset:32 nt
	global_load_dwordx4 v[122:125], v[4:5], off offset:64 nt
	global_load_dwordx4 v[126:129], v[4:5], off offset:0x60 nt
	global_load_dwordx4 v[130:133], v[4:5], off offset:0x80 nt
	global_load_dwordx4 v[134:137], v[4:5], off offset:0xa0 nt
	global_load_dwordx4 v[138:141], v[4:5], off offset:0xc0 nt
	global_load_dwordx4 v[142:145], v[4:5], off offset:0xe0 nt
	s_lshl_b32 s5, s85, 6
	v_lshl_add_u64 v[2:3], v[2:3], 3, s[76:77]
	v_add_u32_e32 v204, 0xffffff80, v11
	s_and_b32 s5, s5, 0x300
	global_load_dwordx2 v[180:181], v[2:3], off nt
	v_add_u32_e32 v3, s75, v204
	s_add_u32 s78, s9, s5
	v_max_i32_e32 v4, 0, v3
	v_mov_b32_e32 v5, v179
	s_addc_u32 s79, s10, 0
	v_lshlrev_b64 v[4:5], 10, v[4:5]
	v_lshl_add_u64 v[4:5], s[78:79], 0, v[4:5]
	v_lshlrev_b32_e32 v6, 4, v9
	v_mov_b32_e32 v7, v179
	v_lshl_add_u64 v[4:5], v[4:5], 0, v[6:7]
	s_mov_b64 s[80:81], 0x4000000
	s_add_i32 s96, s8, 0
	s_mov_b32 m0, s96
	global_load_lds_dwordx4 v[4:5], off
	v_lshl_add_u64 v[4:5], v[4:5], 0, s[80:81]
	s_add_i32 s5, s96, 0x2000
	s_mov_b32 m0, s5
	global_load_lds_dwordx4 v[4:5], off
	v_max_i32_e32 v4, 0xffffffe0, v3
	v_add_u32_e32 v4, 32, v4
	v_mov_b32_e32 v5, v179
	v_lshlrev_b64 v[4:5], 10, v[4:5]
	v_lshl_add_u64 v[4:5], s[78:79], 0, v[4:5]
	v_lshl_add_u64 v[4:5], v[4:5], 0, v[6:7]
	s_add_i32 s5, s96, 0x4000
	s_mov_b32 m0, s5
	global_load_lds_dwordx4 v[4:5], off
	v_lshl_add_u64 v[4:5], v[4:5], 0, s[80:81]
	s_addk_i32 s5, 0x2000
	s_mov_b32 m0, s5
	global_load_lds_dwordx4 v[4:5], off
	v_max_i32_e32 v4, 0xffffffc0, v3
	v_add_u32_e32 v4, 64, v4
	v_mov_b32_e32 v5, v179
	v_lshlrev_b64 v[4:5], 10, v[4:5]
	v_lshl_add_u64 v[4:5], s[78:79], 0, v[4:5]
	v_lshl_add_u64 v[4:5], v[4:5], 0, v[6:7]
	s_add_i32 s5, s96, 0x8000
	s_mov_b32 m0, s5
	global_load_lds_dwordx4 v[4:5], off
	v_lshl_add_u64 v[4:5], v[4:5], 0, s[80:81]
	s_addk_i32 s5, 0x2000
	s_mov_b32 m0, s5
	global_load_lds_dwordx4 v[4:5], off
	v_max_i32_e32 v4, 0xffffffa0, v3
	v_add_u32_e32 v4, 0x60, v4
	v_mov_b32_e32 v5, v179
	v_lshlrev_b64 v[4:5], 10, v[4:5]
	v_lshl_add_u64 v[4:5], s[78:79], 0, v[4:5]
	v_lshl_add_u64 v[4:5], v[4:5], 0, v[6:7]
	s_add_i32 s5, s96, 0xc000
	s_mov_b32 m0, s5
	global_load_lds_dwordx4 v[4:5], off
	v_lshl_add_u64 v[4:5], v[4:5], 0, s[80:81]
	s_addk_i32 s5, 0x2000
	s_mov_b32 m0, s5
	global_load_lds_dwordx4 v[4:5], off
	v_add_u32_e32 v4, s75, v11
	v_mov_b32_e32 v5, v179
	v_lshlrev_b64 v[4:5], 10, v[4:5]
	v_lshl_add_u64 v[4:5], s[78:79], 0, v[4:5]
	v_lshl_add_u64 v[4:5], v[4:5], 0, v[6:7]
	s_add_i32 s5, s96, 0x10000
	s_mov_b32 m0, s5
	global_load_lds_dwordx4 v[4:5], off
	v_lshl_add_u64 v[4:5], v[4:5], 0, s[80:81]
	v_max_i32_e32 v3, 0xffffff60, v3
	v_or_b32_e32 v14, v12, v8
	s_addk_i32 s5, 0x2000
	s_mov_b32 m0, s5
	global_load_lds_dwordx4 v[4:5], off
	v_add_u32_e32 v4, 0xa0, v3
	v_bitop3_b32 v3, v12, v222, v8 bitop3:0x36
	v_lshlrev_b32_e32 v206, 4, v3
	v_bitop3_b32 v3, v222, v14, 2 bitop3:0x36
	v_lshlrev_b32_e32 v207, 4, v3
	v_bitop3_b32 v3, v222, v14, 4 bitop3:0x36
	v_lshlrev_b32_e32 v208, 4, v3
	v_bitop3_b32 v3, v222, v14, 6 bitop3:0x36
	v_lshlrev_b32_e32 v209, 4, v3
	v_bitop3_b32 v3, v222, v14, 8 bitop3:0x36
	v_lshlrev_b32_e32 v210, 4, v3
	v_bitop3_b32 v3, v222, v14, 10 bitop3:0x36
	v_lshlrev_b32_e32 v211, 4, v3
	v_bitop3_b32 v3, v222, v14, 12 bitop3:0x36
	v_lshlrev_b32_e32 v212, 4, v3
	v_bitop3_b32 v3, v222, v14, 14 bitop3:0x36
	v_lshlrev_b32_e32 v213, 4, v3
	v_or_b32_e32 v3, 1, v10
	v_cmp_lt_u32_e64 s[8:9], v3, v1
	v_or_b32_e32 v3, 2, v10
	v_cmp_lt_u32_e64 s[12:13], v3, v1
	v_cmp_gt_u32_e64 s[14:15], v3, v1
	v_or_b32_e32 v3, 3, v10
	v_cmp_lt_u32_e64 s[16:17], v3, v1
	v_cmp_gt_u32_e64 s[18:19], v3, v1
	v_or_b32_e32 v3, 9, v10
	v_cmp_lt_u32_e64 s[24:25], v3, v1
	v_cmp_gt_u32_e64 s[26:27], v3, v1
	v_or_b32_e32 v3, 10, v10
	v_cmp_lt_u32_e64 s[28:29], v3, v1
	v_cmp_gt_u32_e64 s[30:31], v3, v1
	v_or_b32_e32 v3, 11, v10
	v_cmp_lt_u32_e64 s[34:35], v3, v1
	v_cmp_gt_u32_e64 s[36:37], v3, v1
	v_or_b32_e32 v3, 16, v10
	v_cmp_lt_u32_e64 s[38:39], v3, v1
	v_cmp_gt_u32_e64 s[40:41], v3, v1
	v_or_b32_e32 v3, 17, v10
	v_mov_b32_e32 v5, v179
	v_lshl_add_u64 v[182:183], s[0:1], 0, v[178:179]
	v_cmp_gt_u32_e64 s[0:1], 32, v224
	v_cmp_lt_u32_e64 s[42:43], v3, v1
	v_cmp_gt_u32_e64 s[44:45], v3, v1
	v_or_b32_e32 v3, 18, v10
	v_lshlrev_b64 v[4:5], 10, v[4:5]
	v_writelane_b32 v254, s0, 54
	v_cmp_lt_u32_e64 s[46:47], v3, v1
	v_cmp_gt_u32_e64 s[48:49], v3, v1
	v_or_b32_e32 v3, 19, v10
	v_lshl_add_u64 v[4:5], s[78:79], 0, v[4:5]
	v_writelane_b32 v254, s1, 55
	v_cmp_lt_u32_e64 s[0:1], v10, v1
	v_cmp_lt_u32_e64 s[50:51], v3, v1
	v_cmp_gt_u32_e64 s[52:53], v3, v1
	v_or_b32_e32 v3, 24, v10
	v_lshl_add_u64 v[4:5], v[4:5], 0, v[6:7]
	s_add_i32 s5, s96, 0x14000
	s_mov_b32 m0, s5
	global_load_lds_dwordx4 v[4:5], off
	v_writelane_b32 v254, s0, 56
	v_cmp_lt_u32_e64 s[54:55], v3, v1
	v_cmp_gt_u32_e64 s[56:57], v3, v1
	v_or_b32_e32 v3, 25, v10
	v_lshlrev_b32_e32 v2, 3, v9
	v_lshl_add_u64 v[4:5], v[4:5], 0, s[80:81]
	s_addk_i32 s5, 0x2000
	s_mov_b32 m0, s5
	global_load_lds_dwordx4 v[4:5], off
	v_writelane_b32 v254, s1, 57
	v_cmp_gt_u32_e64 s[0:1], v10, v1
	v_cmp_lt_u32_e64 s[58:59], v3, v1
	v_cmp_gt_u32_e64 s[60:61], v3, v1
	v_or_b32_e32 v3, 26, v10
	v_writelane_b32 v254, s0, 61
	v_cmp_lt_u32_e64 s[62:63], v3, v1
	v_cmp_gt_u32_e64 s[64:65], v3, v1
	v_or_b32_e32 v3, 27, v10
	v_lshlrev_b32_e32 v186, 1, v2
	v_mbcnt_lo_u32_b32 v2, -1, 0
	s_mov_b32 s97, 0
	s_mov_b32 s33, 6
	v_lshl_add_u64 v[184:185], s[2:3], 0, v[178:179]
	v_lshlrev_b32_e32 v205, 8, v1
	v_sub_u32_e32 v214, 0, v10
	v_writelane_b32 v254, s1, 62
	v_cmp_ge_u32_e64 s[10:11], v10, v1
	v_sub_u32_e32 v215, -8, v10
	v_cmp_lt_u32_e64 s[20:21], v13, v1
	v_cmp_gt_u32_e64 s[22:23], v13, v1
	v_xor_b32_e32 v216, -9, v10
	v_xor_b32_e32 v217, -10, v10
	v_xor_b32_e32 v218, -11, v10
	v_sub_u32_e32 v219, -16, v10
	v_xor_b32_e32 v220, 0xffffffef, v10
	v_xor_b32_e32 v221, 0xffffffee, v10
	v_xor_b32_e32 v222, 0xffffffed, v10
	v_sub_u32_e32 v223, 0xffffffe8, v10
	v_xor_b32_e32 v225, 0xffffffe7, v10
	v_xor_b32_e32 v226, 0xffffffe6, v10
	v_xor_b32_e32 v227, 0xffffffe5, v10
	v_cmp_lt_u32_e64 s[66:67], v3, v1
	v_cmp_gt_u32_e64 s[68:69], v3, v1
	v_or_b32_e32 v228, s4, v1
	v_or_b32_e32 v229, 0x100, v1
	s_sub_i32 s84, 0, s70
	v_mov_b32_e32 v230, 0xf149f2ca
	v_mbcnt_hi_u32_b32 v231, -1, v2
	s_mov_b32 s5, 6
	s_mov_b32 s6, 0
	v_mov_b32_e32 v194, 0xf149f2ca
	v_mov_b32_e32 v195, v179
	s_mov_b32 s7, 0
	s_waitcnt vmcnt(0)
	s_branch .LBB0_588

; template <int DIL, bool FIRST, bool LAST>
; DI void attn_phase(Frame& F) {
;     ...
;                         if (mq < 3) ATT_PREFETCH(k, qt + 8); else if (k + 1 < nun) ATT_PREFETCH(k + 1, F.wave);
.LBB0_612:
	v_readlane_b32 s0, v254, 49
	v_readlane_b32 s1, v254, 50
	s_andn2_b64 vcc, exec, s[0:1]
	s_cbranch_vccnz .LBB0_614
	global_load_dwordx4 v[82:85], v[188:189], off offset:0
	global_load_dwordx4 v[86:89], v[188:189], off offset:32
	global_load_dwordx4 v[90:93], v[188:189], off offset:64
	global_load_dwordx4 v[94:97], v[188:189], off offset:0x60
	global_load_dwordx4 v[98:101], v[188:189], off offset:0x80
	global_load_dwordx4 v[102:105], v[188:189], off offset:0xa0
	global_load_dwordx4 v[106:109], v[188:189], off offset:0xc0
	global_load_dwordx4 v[110:113], v[188:189], off offset:0xe0
	global_load_dwordx4 v[114:117], v[190:191], off offset:0 nt
	global_load_dwordx4 v[118:121], v[190:191], off offset:32 nt
	global_load_dwordx4 v[122:125], v[190:191], off offset:64 nt
	global_load_dwordx4 v[126:129], v[190:191], off offset:0x60 nt
	global_load_dwordx4 v[130:133], v[190:191], off offset:0x80 nt
	global_load_dwordx4 v[134:137], v[190:191], off offset:0xa0 nt
	global_load_dwordx4 v[138:141], v[190:191], off offset:0xc0 nt
	global_load_dwordx4 v[142:145], v[190:191], off offset:0xe0 nt
	global_load_dwordx2 v[180:181], v[192:193], off nt

; template <int DIL, bool FIRST, bool LAST>
; DI void attn_phase(Frame& F) {
;     ...
;                         if (mq < 3) ATT_PREFETCH(k, qt + 8); else if (k + 1 < nun) ATT_PREFETCH(k + 1, F.wave);
.LBB0_615:
	v_add_u32_e32 v66, s4, v232
	v_ashrrev_i32_e32 v67, 31, v66
	v_lshl_add_u64 v[66:67], v[66:67], 2, s[82:83]
	v_lshlrev_b64 v[68:69], 8, v[66:67]
	v_lshl_add_u64 v[70:71], v[184:185], 0, v[68:69]
	global_load_dwordx4 v[82:85], v[70:71], off offset:0
	global_load_dwordx4 v[86:89], v[70:71], off offset:32
	global_load_dwordx4 v[90:93], v[70:71], off offset:64
	global_load_dwordx4 v[94:97], v[70:71], off offset:0x60
	global_load_dwordx4 v[98:101], v[70:71], off offset:0x80
	global_load_dwordx4 v[102:105], v[70:71], off offset:0xa0
	global_load_dwordx4 v[106:109], v[70:71], off offset:0xc0
	global_load_dwordx4 v[110:113], v[70:71], off offset:0xe0
	v_lshl_add_u64 v[68:69], v[182:183], 0, v[68:69]
	global_load_dwordx4 v[114:117], v[68:69], off offset:0 nt
	global_load_dwordx4 v[118:121], v[68:69], off offset:32 nt
	global_load_dwordx4 v[122:125], v[68:69], off offset:64 nt
	global_load_dwordx4 v[126:129], v[68:69], off offset:0x60 nt
	global_load_dwordx4 v[130:133], v[68:69], off offset:0x80 nt
	global_load_dwordx4 v[134:137], v[68:69], off offset:0xa0 nt
	global_load_dwordx4 v[138:141], v[68:69], off offset:0xc0 nt
	global_load_dwordx4 v[142:145], v[68:69], off offset:0xe0 nt
	v_lshl_add_u64 v[66:67], v[66:67], 3, s[76:77]
	global_load_dwordx2 v[180:181], v[66:67], off nt
	s_branch .LBB0_589
